# baseline (speedup 1.0000x reference)
.LBB12_3:
	s_or_b64 exec, exec, s[4:5]
	s_waitcnt vmcnt(32)
	v_lshl_add_u64 v[28:29], s[20:21], 0, v[8:9]
	v_lshl_add_u64 v[30:31], s[20:21], 0, v[14:15]
	v_lshl_add_u64 v[32:33], s[20:21], 0, v[16:17]
	v_lshl_add_u64 v[34:35], s[20:21], 0, v[12:13]
	v_lshl_add_u64 v[36:37], s[20:21], 0, v[10:11]
	v_lshl_add_u64 v[38:39], s[20:21], 0, v[6:7]
	v_lshl_add_u64 v[40:41], s[20:21], 0, v[4:5]
	v_lshl_add_u64 v[42:43], s[20:21], 0, v[2:3]
	global_load_dword v104, v[28:29], off offset:-1024
	global_load_dword v105, v[28:29], off
	global_load_dword v106, v[30:31], off offset:-1024
	global_load_dword v107, v[30:31], off
	global_load_dword v108, v[32:33], off offset:-1024
	global_load_dword v109, v[32:33], off
	global_load_dword v110, v[34:35], off offset:-1024
	global_load_dword v111, v[34:35], off
	global_load_dword v112, v[36:37], off offset:-1024
	global_load_dword v113, v[36:37], off
	global_load_dword v114, v[38:39], off offset:-1024
	global_load_dword v115, v[38:39], off
	global_load_dword v116, v[40:41], off offset:-1024
	global_load_dword v117, v[40:41], off
	global_load_dword v118, v[42:43], off offset:-1024
	global_load_dword v119, v[42:43], off
	s_add_u32 s20, s20, 0x4000
	s_addc_u32 s21, s21, 0
	s_waitcnt lgkmcnt(0)
	s_barrier
	ds_read_b128 v[28:31], v25 offset:0
	ds_read_b128 v[32:35], v25 offset:16
	ds_read_b128 v[36:39], v25 offset:32
	ds_read_b128 v[40:43], v25 offset:48
	ds_read_b128 v[44:47], v25 offset:1024
	ds_read_b128 v[48:51], v25 offset:1040
	ds_read_b128 v[52:55], v25 offset:1056
	ds_read_b128 v[120:123], v25 offset:1072
	s_waitcnt vmcnt(48) lgkmcnt(0)
	v_pk_fma_f32 v[20:21], v[56:57], v[28:29], v[20:21]
	v_pk_fma_f32 v[18:19], v[56:57], v[44:45], v[18:19]
	v_pk_fma_f32 v[20:21], v[58:59], v[30:31], v[20:21]
	v_pk_fma_f32 v[18:19], v[58:59], v[46:47], v[18:19]
	v_pk_fma_f32 v[20:21], v[60:61], v[32:33], v[20:21]
	v_pk_fma_f32 v[18:19], v[60:61], v[48:49], v[18:19]
	v_pk_fma_f32 v[20:21], v[62:63], v[34:35], v[20:21]
	v_pk_fma_f32 v[18:19], v[62:63], v[50:51], v[18:19]
	v_pk_fma_f32 v[20:21], v[64:65], v[36:37], v[20:21]
	v_pk_fma_f32 v[18:19], v[64:65], v[52:53], v[18:19]
	v_pk_fma_f32 v[20:21], v[66:67], v[38:39], v[20:21]
	v_pk_fma_f32 v[18:19], v[66:67], v[54:55], v[18:19]
	v_pk_fma_f32 v[20:21], v[68:69], v[40:41], v[20:21]
	v_pk_fma_f32 v[18:19], v[68:69], v[120:121], v[18:19]
	v_pk_fma_f32 v[20:21], v[70:71], v[42:43], v[20:21]
	v_pk_fma_f32 v[18:19], v[70:71], v[122:123], v[18:19]
	ds_read_b128 v[28:31], v25 offset:64
	ds_read_b128 v[32:35], v25 offset:80
	ds_read_b128 v[36:39], v25 offset:96
	ds_read_b128 v[40:43], v25 offset:112
	ds_read_b128 v[44:47], v25 offset:1088
	ds_read_b128 v[48:51], v25 offset:1104
	ds_read_b128 v[52:55], v25 offset:1120
	ds_read_b128 v[120:123], v25 offset:1136
	s_waitcnt vmcnt(32) lgkmcnt(0)
	v_pk_fma_f32 v[20:21], v[72:73], v[28:29], v[20:21]
	v_pk_fma_f32 v[18:19], v[72:73], v[44:45], v[18:19]
	v_pk_fma_f32 v[20:21], v[74:75], v[30:31], v[20:21]
	v_pk_fma_f32 v[18:19], v[74:75], v[46:47], v[18:19]
	v_pk_fma_f32 v[20:21], v[76:77], v[32:33], v[20:21]
	v_pk_fma_f32 v[18:19], v[76:77], v[48:49], v[18:19]
	v_pk_fma_f32 v[20:21], v[78:79], v[34:35], v[20:21]
	v_pk_fma_f32 v[18:19], v[78:79], v[50:51], v[18:19]
	v_pk_fma_f32 v[20:21], v[80:81], v[36:37], v[20:21]
	v_pk_fma_f32 v[18:19], v[80:81], v[52:53], v[18:19]
	v_pk_fma_f32 v[20:21], v[82:83], v[38:39], v[20:21]
	v_pk_fma_f32 v[18:19], v[82:83], v[54:55], v[18:19]
	v_pk_fma_f32 v[20:21], v[84:85], v[40:41], v[20:21]
	v_pk_fma_f32 v[18:19], v[84:85], v[120:121], v[18:19]
	v_pk_fma_f32 v[20:21], v[86:87], v[42:43], v[20:21]
	v_pk_fma_f32 v[18:19], v[86:87], v[122:123], v[18:19]
	ds_read_b128 v[28:31], v25 offset:128
	ds_read_b128 v[32:35], v25 offset:144
	ds_read_b128 v[36:39], v25 offset:160
	ds_read_b128 v[40:43], v25 offset:176
	ds_read_b128 v[44:47], v25 offset:1152
	ds_read_b128 v[48:51], v25 offset:1168
	ds_read_b128 v[52:55], v25 offset:1184
	ds_read_b128 v[120:123], v25 offset:1200
	s_waitcnt vmcnt(16) lgkmcnt(0)
	v_pk_fma_f32 v[20:21], v[88:89], v[28:29], v[20:21]
	v_pk_fma_f32 v[18:19], v[88:89], v[44:45], v[18:19]
	v_pk_fma_f32 v[20:21], v[90:91], v[30:31], v[20:21]
	v_pk_fma_f32 v[18:19], v[90:91], v[46:47], v[18:19]
	v_pk_fma_f32 v[20:21], v[92:93], v[32:33], v[20:21]
	v_pk_fma_f32 v[18:19], v[92:93], v[48:49], v[18:19]
	v_pk_fma_f32 v[20:21], v[94:95], v[34:35], v[20:21]
	v_pk_fma_f32 v[18:19], v[94:95], v[50:51], v[18:19]
	v_pk_fma_f32 v[20:21], v[96:97], v[36:37], v[20:21]
	v_pk_fma_f32 v[18:19], v[96:97], v[52:53], v[18:19]
	v_pk_fma_f32 v[20:21], v[98:99], v[38:39], v[20:21]
	v_pk_fma_f32 v[18:19], v[98:99], v[54:55], v[18:19]
	v_pk_fma_f32 v[20:21], v[100:101], v[40:41], v[20:21]
	v_pk_fma_f32 v[18:19], v[100:101], v[120:121], v[18:19]
	v_pk_fma_f32 v[20:21], v[102:103], v[42:43], v[20:21]
	v_pk_fma_f32 v[18:19], v[102:103], v[122:123], v[18:19]
	ds_read_b128 v[28:31], v25 offset:192
	ds_read_b128 v[32:35], v25 offset:208
	ds_read_b128 v[36:39], v25 offset:224
	ds_read_b128 v[40:43], v25 offset:240
	ds_read_b128 v[44:47], v25 offset:1216
	ds_read_b128 v[48:51], v25 offset:1232
	ds_read_b128 v[52:55], v25 offset:1248
	ds_read_b128 v[120:123], v25 offset:1264
	s_waitcnt vmcnt(0) lgkmcnt(0)
	v_pk_fma_f32 v[20:21], v[104:105], v[28:29], v[20:21]
	v_pk_fma_f32 v[18:19], v[104:105], v[44:45], v[18:19]
	v_pk_fma_f32 v[20:21], v[106:107], v[30:31], v[20:21]
	v_pk_fma_f32 v[18:19], v[106:107], v[46:47], v[18:19]
	v_pk_fma_f32 v[20:21], v[108:109], v[32:33], v[20:21]
	v_pk_fma_f32 v[18:19], v[108:109], v[48:49], v[18:19]
	v_pk_fma_f32 v[20:21], v[110:111], v[34:35], v[20:21]
	v_pk_fma_f32 v[18:19], v[110:111], v[50:51], v[18:19]
	v_pk_fma_f32 v[20:21], v[112:113], v[36:37], v[20:21]
	v_pk_fma_f32 v[18:19], v[112:113], v[52:53], v[18:19]
	v_pk_fma_f32 v[20:21], v[114:115], v[38:39], v[20:21]
	v_pk_fma_f32 v[18:19], v[114:115], v[54:55], v[18:19]
	v_pk_fma_f32 v[20:21], v[116:117], v[40:41], v[20:21]
	v_pk_fma_f32 v[18:19], v[116:117], v[120:121], v[18:19]
	v_pk_fma_f32 v[20:21], v[118:119], v[42:43], v[20:21]
	v_pk_fma_f32 v[18:19], v[118:119], v[122:123], v[18:19]
	s_or_b64 exec, exec, s[4:5]
	v_add_f32_e32 v20, v20, v21
	v_mov_b32_e32 v21, 2
	v_lshlrev_b32_sdwa v26, v21, v0 dst_sel:DWORD dst_unused:UNUSED_PAD src0_sel:DWORD src1_sel:BYTE_0
	v_lshl_or_b32 v25, v1, 10, v26
	v_add_f32_e32 v18, v18, v19
	s_movk_i32 s3, 0x100
	ds_write2st64_b32 v25, v20, v18 offset1:16
	v_cmp_gt_u32_e64 s[4:5], s3, v0
	v_lshl_or_b32 v18, s2, 8, v0
	s_waitcnt lgkmcnt(0)
	s_barrier
	s_and_saveexec_b64 s[20:21], s[4:5]
	s_cbranch_execz .LBB12_7
	v_lshl_or_b32 v20, s2, 11, v0
	s_lshl_b32 s2, s2, 13
	s_and_b32 s2, s2, 0xe000
	v_lshl_or_b32 v28, v0, 2, s2
	v_mov_b32_e32 v29, 0
	s_movk_i32 s3, 0x1000
	v_lshl_add_u64 v[30:31], s[12:13], 0, v[28:29]
	v_add_co_u32_e32 v32, vcc, s3, v30
	s_mov_b32 s2, 0x10000
	s_nop 0
	v_addc_co_u32_e32 v33, vcc, 0, v31, vcc
	v_add_co_u32_e32 v34, vcc, s2, v30
	s_mov_b32 s2, 0x11000
	s_nop 0
	v_addc_co_u32_e32 v35, vcc, 0, v31, vcc
	v_add_co_u32_e32 v36, vcc, s2, v30
	s_mov_b32 s2, 0x20000
	s_nop 0
	v_addc_co_u32_e32 v37, vcc, 0, v31, vcc
	v_add_co_u32_e32 v38, vcc, s2, v30
	v_ashrrev_i32_e32 v21, 31, v20
	s_nop 0
	v_addc_co_u32_e32 v39, vcc, 0, v31, vcc
	s_mov_b32 s2, 0x21000
	v_lshl_add_u64 v[20:21], v[20:21], 2, s[12:13]
	v_add_co_u32_e32 v40, vcc, s2, v30
	global_load_dword v19, v[20:21], off
	global_load_dword v27, v[20:21], off offset:1024
	v_addc_co_u32_e32 v41, vcc, 0, v31, vcc
	global_load_dword v42, v[32:33], off
	global_load_dword v43, v[32:33], off offset:1024
	global_load_dword v44, v[32:33], off offset:2048
	global_load_dword v45, v[32:33], off offset:3072
	global_load_dword v46, v[34:35], off offset:1024
	global_load_dword v47, v[34:35], off offset:2048
	global_load_dword v48, v[34:35], off offset:3072
	global_load_dword v49, v[38:39], off offset:1024
	global_load_dword v50, v28, s[12:13]
	global_load_dword v51, v28, s[12:13] offset:1024
	global_load_dword v52, v28, s[12:13] offset:2048
	global_load_dword v53, v[38:39], off offset:2048
	global_load_dword v54, v[38:39], off offset:3072
	global_load_dword v55, v28, s[12:13] offset:3072
	global_load_dword v56, v[36:37], off offset:-4096
	global_load_dword v33, v[36:37], off
	global_load_dword v35, v[36:37], off offset:1024
	s_nop 0
	global_load_dword v38, v[36:37], off offset:2048
	global_load_dword v39, v[36:37], off offset:3072
	global_load_dword v57, v[40:41], off offset:-4096
	global_load_dword v58, v[40:41], off
	s_mov_b32 s2, 0x30000
	v_add_co_u32_e32 v28, vcc, s2, v30
	s_mov_b32 s2, 0x31000
	s_nop 0
	v_addc_co_u32_e32 v29, vcc, 0, v31, vcc
	v_add_co_u32_e32 v30, vcc, s2, v30
	s_waitcnt vmcnt(22)
	v_add_f32_e32 v19, 0, v19
	v_addc_co_u32_e32 v31, vcc, 0, v31, vcc
	global_load_dword v37, v[40:41], off offset:1024
	global_load_dword v59, v[40:41], off offset:2048
	global_load_dword v60, v[40:41], off offset:3072
	global_load_dword v61, v[30:31], off offset:-4096
	global_load_dword v62, v[28:29], off offset:1024
	global_load_dword v63, v[28:29], off offset:2048
	global_load_dword v64, v[28:29], off offset:3072
	global_load_dword v65, v[30:31], off
	v_add_co_u32_e32 v28, vcc, 0x1000, v20
	s_waitcnt vmcnt(29)
	v_add_f32_e32 v19, v19, v27
	v_addc_co_u32_e32 v29, vcc, 0, v21, vcc
	global_load_dword v66, v[20:21], off offset:2048
	global_load_dword v67, v[20:21], off offset:3072
	global_load_dword v68, v[28:29], off
	s_nop 0
	global_load_dword v20, v[28:29], off offset:1024
	global_load_dword v32, v[28:29], off offset:2048
	s_nop 0
	global_load_dword v28, v[28:29], off offset:3072
	s_nop 0
	global_load_dword v29, v26, s[6:7]
	global_load_dword v34, v[30:31], off offset:1024
	global_load_dword v36, v[30:31], off offset:2048
	s_nop 0
	global_load_dword v30, v[30:31], off offset:3072
	s_waitcnt vmcnt(30)
	v_add_f32_e32 v21, 0, v50
	s_waitcnt vmcnt(29)
	v_add_f32_e32 v21, v21, v51
	s_waitcnt vmcnt(28)
	v_add_f32_e32 v21, v21, v52
	s_waitcnt vmcnt(25)
	v_add_f32_e32 v21, v21, v55
	v_add_f32_e32 v21, v21, v42
	v_add_f32_e32 v21, v21, v43
	v_add_f32_e32 v21, v21, v44
	v_add_f32_e32 v21, v21, v45
	s_waitcnt vmcnt(24)
	v_add_f32_e32 v21, v21, v56
	v_add_f32_e32 v21, v21, v46
	v_add_f32_e32 v21, v21, v47
	v_add_f32_e32 v21, v21, v48
	s_waitcnt vmcnt(23)
	v_add_f32_e32 v21, v21, v33
	s_waitcnt vmcnt(22)
	v_add_f32_e32 v21, v21, v35
	s_waitcnt vmcnt(21)
	v_add_f32_e32 v21, v21, v38
	s_waitcnt vmcnt(20)
	v_add_f32_e32 v21, v21, v39
	s_waitcnt vmcnt(19)
	v_add_f32_e32 v21, v21, v57
	v_add_f32_e32 v21, v21, v49
	v_add_f32_e32 v21, v21, v53
	v_add_f32_e32 v21, v21, v54
	s_waitcnt vmcnt(18)
	v_add_f32_e32 v21, v21, v58
	ds_read2st64_b32 v[40:41], v26 offset0:8 offset1:12
	ds_read2st64_b32 v[42:43], v26 offset1:4
	s_waitcnt lgkmcnt(1)
	v_add_f32_e32 v33, v40, v41
	s_waitcnt lgkmcnt(0)
	v_mov_b32_e32 v45, v42
	s_waitcnt vmcnt(17)
	v_add_f32_e32 v21, v21, v37
	s_waitcnt vmcnt(16)
	v_add_f32_e32 v21, v21, v59
	s_waitcnt vmcnt(15)
	v_add_f32_e32 v21, v21, v60
	s_waitcnt vmcnt(14)
	v_add_f32_e32 v21, v21, v61
	s_waitcnt vmcnt(13)
	v_add_f32_e32 v21, v21, v62
	s_waitcnt vmcnt(12)
	v_add_f32_e32 v21, v21, v63
	s_waitcnt vmcnt(11)
	v_add_f32_e32 v21, v21, v64
	s_waitcnt vmcnt(10)
	v_add_f32_e32 v38, v21, v65
	s_waitcnt vmcnt(9)
	v_add_f32_e32 v19, v19, v66
	v_mov_b32_e32 v21, v43
	ds_read2st64_b32 v[40:41], v26 offset0:24 offset1:28
	ds_read2st64_b32 v[42:43], v26 offset0:16 offset1:20
	s_waitcnt vmcnt(8)
	v_add_f32_e32 v19, v19, v67
	s_waitcnt vmcnt(7)
	v_add_f32_e32 v44, v19, v68
	s_waitcnt vmcnt(6)
	v_pk_add_f32 v[20:21], v[44:45], v[20:21]
	s_waitcnt lgkmcnt(1)
	v_add_f32_e32 v37, v40, v41
	s_waitcnt vmcnt(5)
	v_pk_add_f32 v[20:21], v[20:21], v[32:33]
	s_waitcnt lgkmcnt(0)
	v_mov_b32_e32 v39, v42
	s_waitcnt vmcnt(3)
	v_pk_add_f32 v[20:21], v[20:21], v[28:29]
	v_mov_b32_e32 v35, v43
	v_fmamk_f32 v27, v20, 0x3a800000, v21
	s_waitcnt vmcnt(2)
	v_pk_add_f32 v[20:21], v[38:39], v[34:35]
	v_mov_b32_e32 v31, v29
	s_waitcnt vmcnt(1)
	v_pk_add_f32 v[20:21], v[20:21], v[36:37]
	v_ashrrev_i32_e32 v19, 31, v18
	s_waitcnt vmcnt(0)
	v_pk_add_f32 v[20:21], v[20:21], v[30:31]
	s_nop 0
	v_fmamk_f32 v28, v20, 0x39800000, v21
	v_lshl_add_u64 v[20:21], v[18:19], 2, s[14:15]
	global_store_dword v[20:21], v27, off
	ds_write_b32 v26, v28 offset:10240
.LBB12_7:
	s_or_b64 exec, exec, s[20:21]
	v_mov_b32_e32 v20, 0
	v_or_b32_e32 v19, 0x2800, v24
	s_mov_b64 s[2:3], 0
	s_mov_b64 s[12:13], s[10:11]
	v_mov_b32_e32 v24, v22
	v_mov_b32_e32 v21, v20
	s_waitcnt lgkmcnt(0)
	s_barrier
	v_lshl_add_u64 v[26:27], s[12:13], 0, v[8:9]
	v_lshl_add_u64 v[28:29], s[12:13], 0, v[14:15]
	v_lshl_add_u64 v[30:31], s[12:13], 0, v[16:17]
	v_lshl_add_u64 v[32:33], s[12:13], 0, v[12:13]
	v_lshl_add_u64 v[34:35], s[12:13], 0, v[10:11]
	v_lshl_add_u64 v[36:37], s[12:13], 0, v[6:7]
	v_lshl_add_u64 v[38:39], s[12:13], 0, v[4:5]
	v_lshl_add_u64 v[40:41], s[12:13], 0, v[2:3]
	global_load_dword v42, v[26:27], off offset:-1024
	global_load_dword v43, v[26:27], off
	global_load_dword v44, v[28:29], off offset:-1024
	global_load_dword v45, v[28:29], off
	global_load_dword v46, v[30:31], off offset:-1024
	global_load_dword v47, v[30:31], off
	global_load_dword v48, v[32:33], off offset:-1024
	global_load_dword v49, v[32:33], off
	global_load_dword v50, v[34:35], off offset:-1024
	global_load_dword v51, v[34:35], off
	global_load_dword v52, v[36:37], off offset:-1024
	global_load_dword v53, v[36:37], off
	global_load_dword v54, v[38:39], off offset:-1024
	global_load_dword v55, v[38:39], off
	global_load_dword v56, v[40:41], off offset:-1024
	global_load_dword v57, v[40:41], off
	s_add_u32 s12, s12, 0x4000
	s_addc_u32 s13, s13, 0
	v_lshl_add_u64 v[26:27], s[12:13], 0, v[8:9]
	v_lshl_add_u64 v[28:29], s[12:13], 0, v[14:15]
	v_lshl_add_u64 v[30:31], s[12:13], 0, v[16:17]
	v_lshl_add_u64 v[32:33], s[12:13], 0, v[12:13]
	v_lshl_add_u64 v[34:35], s[12:13], 0, v[10:11]
	v_lshl_add_u64 v[36:37], s[12:13], 0, v[6:7]
	v_lshl_add_u64 v[38:39], s[12:13], 0, v[4:5]
	v_lshl_add_u64 v[40:41], s[12:13], 0, v[2:3]
	global_load_dword v72, v[26:27], off offset:-1024
	global_load_dword v73, v[26:27], off
	global_load_dword v74, v[28:29], off offset:-1024
	global_load_dword v75, v[28:29], off
	global_load_dword v76, v[30:31], off offset:-1024
	global_load_dword v77, v[30:31], off
	global_load_dword v78, v[32:33], off offset:-1024
	global_load_dword v79, v[32:33], off
	global_load_dword v80, v[34:35], off offset:-1024
	global_load_dword v81, v[34:35], off
	global_load_dword v82, v[36:37], off offset:-1024
	global_load_dword v83, v[36:37], off
	global_load_dword v84, v[38:39], off offset:-1024
	global_load_dword v85, v[38:39], off
	global_load_dword v86, v[40:41], off offset:-1024
	global_load_dword v87, v[40:41], off
	s_add_u32 s12, s12, 0x4000
	s_addc_u32 s13, s13, 0
	v_lshl_add_u64 v[26:27], s[12:13], 0, v[8:9]
	v_lshl_add_u64 v[28:29], s[12:13], 0, v[14:15]
	v_lshl_add_u64 v[30:31], s[12:13], 0, v[16:17]
	v_lshl_add_u64 v[32:33], s[12:13], 0, v[12:13]
	v_lshl_add_u64 v[34:35], s[12:13], 0, v[10:11]
	v_lshl_add_u64 v[36:37], s[12:13], 0, v[6:7]
	v_lshl_add_u64 v[38:39], s[12:13], 0, v[4:5]
	v_lshl_add_u64 v[40:41], s[12:13], 0, v[2:3]
	global_load_dword v88, v[26:27], off offset:-1024
	global_load_dword v89, v[26:27], off
	global_load_dword v90, v[28:29], off offset:-1024
	global_load_dword v91, v[28:29], off
	global_load_dword v92, v[30:31], off offset:-1024
	global_load_dword v93, v[30:31], off
	global_load_dword v94, v[32:33], off offset:-1024
	global_load_dword v95, v[32:33], off
	global_load_dword v96, v[34:35], off offset:-1024
	global_load_dword v97, v[34:35], off
	global_load_dword v98, v[36:37], off offset:-1024
	global_load_dword v99, v[36:37], off
	global_load_dword v100, v[38:39], off offset:-1024
	global_load_dword v101, v[38:39], off
	global_load_dword v102, v[40:41], off offset:-1024
	global_load_dword v103, v[40:41], off
	s_add_u32 s12, s12, 0x4000
	s_addc_u32 s13, s13, 0
	s_waitcnt vmcnt(32)
	v_lshl_add_u64 v[26:27], s[12:13], 0, v[8:9]
	v_lshl_add_u64 v[28:29], s[12:13], 0, v[14:15]
	v_lshl_add_u64 v[30:31], s[12:13], 0, v[16:17]
	v_lshl_add_u64 v[32:33], s[12:13], 0, v[12:13]
	v_lshl_add_u64 v[34:35], s[12:13], 0, v[10:11]
	v_lshl_add_u64 v[36:37], s[12:13], 0, v[6:7]
	v_lshl_add_u64 v[38:39], s[12:13], 0, v[4:5]
	v_lshl_add_u64 v[40:41], s[12:13], 0, v[2:3]
	global_load_dword v104, v[26:27], off offset:-1024
	global_load_dword v105, v[26:27], off
	global_load_dword v106, v[28:29], off offset:-1024
	global_load_dword v107, v[28:29], off
	global_load_dword v108, v[30:31], off offset:-1024
	global_load_dword v109, v[30:31], off
	global_load_dword v110, v[32:33], off offset:-1024
	global_load_dword v111, v[32:33], off
	global_load_dword v112, v[34:35], off offset:-1024
	global_load_dword v113, v[34:35], off
	global_load_dword v114, v[36:37], off offset:-1024
	global_load_dword v115, v[36:37], off
	global_load_dword v116, v[38:39], off offset:-1024
	global_load_dword v117, v[38:39], off
	global_load_dword v118, v[40:41], off offset:-1024
	global_load_dword v119, v[40:41], off
	s_add_u32 s12, s12, 0x4000
	s_addc_u32 s13, s13, 0
	ds_read_b128 v[26:29], v19 offset:0
	ds_read_b128 v[30:33], v19 offset:16
	ds_read_b128 v[34:37], v19 offset:32
	ds_read_b128 v[38:41], v19 offset:48
	s_waitcnt vmcnt(48) lgkmcnt(0)
	v_pk_fma_f32 v[20:21], v[42:43], v[26:27], v[20:21]
	v_pk_fma_f32 v[20:21], v[44:45], v[28:29], v[20:21]
	v_pk_fma_f32 v[20:21], v[46:47], v[30:31], v[20:21]
	v_pk_fma_f32 v[20:21], v[48:49], v[32:33], v[20:21]
	v_pk_fma_f32 v[20:21], v[50:51], v[34:35], v[20:21]
	v_pk_fma_f32 v[20:21], v[52:53], v[36:37], v[20:21]
	v_pk_fma_f32 v[20:21], v[54:55], v[38:39], v[20:21]
	v_pk_fma_f32 v[20:21], v[56:57], v[40:41], v[20:21]
	ds_read_b128 v[26:29], v19 offset:64
	ds_read_b128 v[30:33], v19 offset:80
	ds_read_b128 v[34:37], v19 offset:96
	ds_read_b128 v[38:41], v19 offset:112
	s_waitcnt vmcnt(32) lgkmcnt(0)
	v_pk_fma_f32 v[20:21], v[72:73], v[26:27], v[20:21]
	v_pk_fma_f32 v[20:21], v[74:75], v[28:29], v[20:21]
	v_pk_fma_f32 v[20:21], v[76:77], v[30:31], v[20:21]
	v_pk_fma_f32 v[20:21], v[78:79], v[32:33], v[20:21]
	v_pk_fma_f32 v[20:21], v[80:81], v[34:35], v[20:21]
	v_pk_fma_f32 v[20:21], v[82:83], v[36:37], v[20:21]
	v_pk_fma_f32 v[20:21], v[84:85], v[38:39], v[20:21]
	v_pk_fma_f32 v[20:21], v[86:87], v[40:41], v[20:21]
	ds_read_b128 v[26:29], v19 offset:128
	ds_read_b128 v[30:33], v19 offset:144
	ds_read_b128 v[34:37], v19 offset:160
	ds_read_b128 v[38:41], v19 offset:176
	s_waitcnt vmcnt(16) lgkmcnt(0)
	v_pk_fma_f32 v[20:21], v[88:89], v[26:27], v[20:21]
	v_pk_fma_f32 v[20:21], v[90:91], v[28:29], v[20:21]
	v_pk_fma_f32 v[20:21], v[92:93], v[30:31], v[20:21]
	v_pk_fma_f32 v[20:21], v[94:95], v[32:33], v[20:21]
	v_pk_fma_f32 v[20:21], v[96:97], v[34:35], v[20:21]
	v_pk_fma_f32 v[20:21], v[98:99], v[36:37], v[20:21]
	v_pk_fma_f32 v[20:21], v[100:101], v[38:39], v[20:21]
	v_pk_fma_f32 v[20:21], v[102:103], v[40:41], v[20:21]
	ds_read_b128 v[26:29], v19 offset:192
	ds_read_b128 v[30:33], v19 offset:208
	ds_read_b128 v[34:37], v19 offset:224
	ds_read_b128 v[38:41], v19 offset:240
	s_waitcnt vmcnt(0) lgkmcnt(0)
	v_pk_fma_f32 v[20:21], v[104:105], v[26:27], v[20:21]
	v_pk_fma_f32 v[20:21], v[106:107], v[28:29], v[20:21]
	v_pk_fma_f32 v[20:21], v[108:109], v[30:31], v[20:21]
	v_pk_fma_f32 v[20:21], v[110:111], v[32:33], v[20:21]
	v_pk_fma_f32 v[20:21], v[112:113], v[34:35], v[20:21]
	v_pk_fma_f32 v[20:21], v[114:115], v[36:37], v[20:21]
	v_pk_fma_f32 v[20:21], v[116:117], v[38:39], v[20:21]
	v_pk_fma_f32 v[20:21], v[118:119], v[40:41], v[20:21]
	s_or_b64 exec, exec, s[2:3]
	v_add_f32_e32 v2, v20, v21
	ds_write_b32 v25, v2
	s_waitcnt lgkmcnt(0)
	s_barrier
	s_and_saveexec_b64 s[2:3], s[4:5]
	s_cbranch_execz .LBB12_11
	v_mov_b32_e32 v2, 2
	v_lshlrev_b32_sdwa v4, v2, v0 dst_sel:DWORD dst_unused:UNUSED_PAD src0_sel:DWORD src1_sel:BYTE_0
	ds_read2st64_b32 v[2:3], v4 offset1:4
	ds_read2st64_b32 v[4:5], v4 offset0:8 offset1:12
	v_ashrrev_i32_e32 v19, 31, v18
	s_waitcnt lgkmcnt(1)
	v_mov_b32_e32 v6, v2
	s_waitcnt lgkmcnt(0)
	v_mov_b32_e32 v7, v4
	v_mov_b32_e32 v4, v3
	v_pk_add_f32 v[2:3], v[6:7], v[4:5]
	s_nop 0
	v_add_f32_e32 v4, v2, v3
	v_lshl_add_u64 v[2:3], v[18:19], 2, s[18:19]
	global_store_dword v[2:3], v4, off

.LBB12_12:
	s_and_b64 vcc, exec, s[4:5]
	s_cbranch_vccz .LBB12_23
	s_load_dwordx2 s[4:5], s[0:1], 0x48
	s_load_dwordx2 s[2:3], s[0:1], 0x38
	v_lshlrev_b32_e32 v2, 14, v1
	v_or_b32_e32 v3, v0, v2
	v_or_b32_sdwa v2, v2, v0 dst_sel:DWORD dst_unused:UNUSED_PAD src0_sel:DWORD src1_sel:BYTE_0
	v_lshlrev_b32_e32 v2, 2, v2
	v_mov_b32_e32 v5, 0
	v_lshlrev_b32_e32 v16, 2, v3
	v_add_u32_e32 v23, 64, v22
	v_or_b32_e32 v4, 0x3000, v2
	v_or_b32_e32 v8, 0x3c00, v16
	v_mov_b32_e32 v9, v5
	v_or_b32_e32 v10, 0x2000, v2
	v_mov_b32_e32 v11, v5
	v_mov_b32_e32 v3, v5
	v_or_b32_e32 v12, 0x2c00, v16
	v_mov_b32_e32 v13, v5
	v_or_b32_e32 v6, 0x1000, v2
	v_mov_b32_e32 v7, v5
	v_or_b32_e32 v14, 0x1c00, v16
	v_mov_b32_e32 v15, v5
	v_or_b32_e32 v16, 0xc00, v16
	v_mov_b32_e32 v17, v5
	s_mov_b64 s[0:1], 0
	v_mov_b32_e32 v24, v22
	v_mov_b32_e32 v18, v5
	v_mov_b32_e32 v19, v5
	v_mov_b32_e32 v20, v5
	v_mov_b32_e32 v21, v5
	s_waitcnt lgkmcnt(0)
	v_lshl_add_u64 v[26:27], s[10:11], 0, v[2:3]
	v_lshl_add_u64 v[28:29], s[10:11], 0, v[16:17]
	v_lshl_add_u64 v[30:31], s[10:11], 0, v[6:7]
	v_lshl_add_u64 v[32:33], s[10:11], 0, v[14:15]
	v_lshl_add_u64 v[34:35], s[10:11], 0, v[10:11]
	v_lshl_add_u64 v[36:37], s[10:11], 0, v[12:13]
	v_lshl_add_u64 v[38:39], s[10:11], 0, v[4:5]
	v_lshl_add_u64 v[40:41], s[10:11], 0, v[8:9]
	global_load_dword v43, v[26:27], off
	global_load_dword v45, v[26:27], off offset:1024
	global_load_dword v44, v[26:27], off offset:2048
	global_load_dword v42, v[28:29], off
	global_load_dword v47, v[30:31], off
	global_load_dword v49, v[30:31], off offset:1024
	global_load_dword v48, v[30:31], off offset:2048
	global_load_dword v46, v[32:33], off
	global_load_dword v51, v[34:35], off
	global_load_dword v53, v[34:35], off offset:1024
	global_load_dword v52, v[34:35], off offset:2048
	global_load_dword v50, v[36:37], off
	global_load_dword v55, v[38:39], off
	global_load_dword v57, v[38:39], off offset:1024
	global_load_dword v56, v[38:39], off offset:2048
	global_load_dword v54, v[40:41], off
	s_add_u32 s10, s10, 0x4000
	s_addc_u32 s11, s11, 0
	v_lshl_add_u64 v[26:27], s[10:11], 0, v[2:3]
	v_lshl_add_u64 v[28:29], s[10:11], 0, v[16:17]
	v_lshl_add_u64 v[30:31], s[10:11], 0, v[6:7]
	v_lshl_add_u64 v[32:33], s[10:11], 0, v[14:15]
	v_lshl_add_u64 v[34:35], s[10:11], 0, v[10:11]
	v_lshl_add_u64 v[36:37], s[10:11], 0, v[12:13]
	v_lshl_add_u64 v[38:39], s[10:11], 0, v[4:5]
	v_lshl_add_u64 v[40:41], s[10:11], 0, v[8:9]
	global_load_dword v73, v[26:27], off
	global_load_dword v75, v[26:27], off offset:1024
	global_load_dword v74, v[26:27], off offset:2048
	global_load_dword v72, v[28:29], off
	global_load_dword v77, v[30:31], off
	global_load_dword v79, v[30:31], off offset:1024
	global_load_dword v78, v[30:31], off offset:2048
	global_load_dword v76, v[32:33], off
	global_load_dword v81, v[34:35], off
	global_load_dword v83, v[34:35], off offset:1024
	global_load_dword v82, v[34:35], off offset:2048
	global_load_dword v80, v[36:37], off
	global_load_dword v85, v[38:39], off
	global_load_dword v87, v[38:39], off offset:1024
	global_load_dword v86, v[38:39], off offset:2048
	global_load_dword v84, v[40:41], off
	s_add_u32 s10, s10, 0x4000
	s_addc_u32 s11, s11, 0
	v_lshl_add_u64 v[26:27], s[10:11], 0, v[2:3]
	v_lshl_add_u64 v[28:29], s[10:11], 0, v[16:17]
	v_lshl_add_u64 v[30:31], s[10:11], 0, v[6:7]
	v_lshl_add_u64 v[32:33], s[10:11], 0, v[14:15]
	v_lshl_add_u64 v[34:35], s[10:11], 0, v[10:11]
	v_lshl_add_u64 v[36:37], s[10:11], 0, v[12:13]
	v_lshl_add_u64 v[38:39], s[10:11], 0, v[4:5]
	v_lshl_add_u64 v[40:41], s[10:11], 0, v[8:9]
	global_load_dword v89, v[26:27], off
	global_load_dword v91, v[26:27], off offset:1024
	global_load_dword v90, v[26:27], off offset:2048
	global_load_dword v88, v[28:29], off
	global_load_dword v93, v[30:31], off
	global_load_dword v95, v[30:31], off offset:1024
	global_load_dword v94, v[30:31], off offset:2048
	global_load_dword v92, v[32:33], off
	global_load_dword v97, v[34:35], off
	global_load_dword v99, v[34:35], off offset:1024
	global_load_dword v98, v[34:35], off offset:2048
	global_load_dword v96, v[36:37], off
	global_load_dword v101, v[38:39], off
	global_load_dword v103, v[38:39], off offset:1024
	global_load_dword v102, v[38:39], off offset:2048
	global_load_dword v100, v[40:41], off
	s_add_u32 s10, s10, 0x4000
	s_addc_u32 s11, s11, 0
	s_waitcnt vmcnt(32)
	v_lshl_add_u64 v[26:27], s[10:11], 0, v[2:3]
	v_lshl_add_u64 v[28:29], s[10:11], 0, v[16:17]
	v_lshl_add_u64 v[30:31], s[10:11], 0, v[6:7]
	v_lshl_add_u64 v[32:33], s[10:11], 0, v[14:15]
	v_lshl_add_u64 v[34:35], s[10:11], 0, v[10:11]
	v_lshl_add_u64 v[36:37], s[10:11], 0, v[12:13]
	v_lshl_add_u64 v[38:39], s[10:11], 0, v[4:5]
	v_lshl_add_u64 v[40:41], s[10:11], 0, v[8:9]
	global_load_dword v105, v[26:27], off
	global_load_dword v107, v[26:27], off offset:1024
	global_load_dword v106, v[26:27], off offset:2048
	global_load_dword v104, v[28:29], off
	global_load_dword v109, v[30:31], off
	global_load_dword v111, v[30:31], off offset:1024
	global_load_dword v110, v[30:31], off offset:2048
	global_load_dword v108, v[32:33], off
	global_load_dword v113, v[34:35], off
	global_load_dword v115, v[34:35], off offset:1024
	global_load_dword v114, v[34:35], off offset:2048
	global_load_dword v112, v[36:37], off
	global_load_dword v117, v[38:39], off
	global_load_dword v119, v[38:39], off offset:1024
	global_load_dword v118, v[38:39], off offset:2048
	global_load_dword v116, v[40:41], off
	s_add_u32 s10, s10, 0x4000
	s_addc_u32 s11, s11, 0
	s_waitcnt vmcnt(48)
	v_pk_add_f32 v[18:19], v[18:19], v[44:45]
	v_pk_add_f32 v[20:21], v[20:21], v[42:43]
	v_pk_add_f32 v[18:19], v[18:19], v[48:49]
	v_pk_add_f32 v[20:21], v[20:21], v[46:47]
	v_pk_add_f32 v[18:19], v[18:19], v[52:53]
	v_pk_add_f32 v[20:21], v[20:21], v[50:51]
	v_pk_add_f32 v[18:19], v[18:19], v[56:57]
	v_pk_add_f32 v[20:21], v[20:21], v[54:55]
	s_waitcnt vmcnt(32)
	v_pk_add_f32 v[18:19], v[18:19], v[74:75]
	v_pk_add_f32 v[20:21], v[20:21], v[72:73]
	v_pk_add_f32 v[18:19], v[18:19], v[78:79]
	v_pk_add_f32 v[20:21], v[20:21], v[76:77]
	v_pk_add_f32 v[18:19], v[18:19], v[82:83]
	v_pk_add_f32 v[20:21], v[20:21], v[80:81]
	v_pk_add_f32 v[18:19], v[18:19], v[86:87]
	v_pk_add_f32 v[20:21], v[20:21], v[84:85]
	s_waitcnt vmcnt(16)
	v_pk_add_f32 v[18:19], v[18:19], v[90:91]
	v_pk_add_f32 v[20:21], v[20:21], v[88:89]
	v_pk_add_f32 v[18:19], v[18:19], v[94:95]
	v_pk_add_f32 v[20:21], v[20:21], v[92:93]
	v_pk_add_f32 v[18:19], v[18:19], v[98:99]
	v_pk_add_f32 v[20:21], v[20:21], v[96:97]
	v_pk_add_f32 v[18:19], v[18:19], v[102:103]
	v_pk_add_f32 v[20:21], v[20:21], v[100:101]
	s_waitcnt vmcnt(0)
	v_pk_add_f32 v[18:19], v[18:19], v[106:107]
	v_pk_add_f32 v[20:21], v[20:21], v[104:105]
	v_pk_add_f32 v[18:19], v[18:19], v[110:111]
	v_pk_add_f32 v[20:21], v[20:21], v[108:109]
	v_pk_add_f32 v[18:19], v[18:19], v[114:115]
	v_pk_add_f32 v[20:21], v[20:21], v[112:113]
	v_pk_add_f32 v[18:19], v[18:19], v[118:119]
	v_pk_add_f32 v[20:21], v[20:21], v[116:117]
	s_or_b64 exec, exec, s[0:1]
	v_pk_add_f32 v[4:5], v[18:19], v[20:21]
	s_mov_b64 s[0:1], 0x400
	v_add_f32_e32 v4, v4, v5
	v_mov_b32_e32 v5, 2
	v_lshlrev_b32_sdwa v5, v5, v0 dst_sel:DWORD dst_unused:UNUSED_PAD src0_sel:DWORD src1_sel:BYTE_0
	v_lshl_or_b32 v14, v1, 10, v5
	ds_write_b32 v14, v4
	v_add_u32_e32 v4, 0x1800, v2
	v_mov_b32_e32 v5, 0
	v_lshl_add_u64 v[8:9], v[4:5], 0, s[0:1]
	v_add_u32_e32 v4, 0x800, v2
	v_lshl_add_u64 v[10:11], v[2:3], 0, s[0:1]
	v_lshl_add_u64 v[2:3], v[4:5], 0, s[0:1]
	v_and_b32_e32 v4, 0x300, v0
	v_lshl_add_u64 v[12:13], s[16:17], 0, v[4:5]
	v_lshl_add_u64 v[6:7], v[6:7], 0, s[0:1]
	v_lshl_add_u64 v[12:13], v[12:13], 0, 16
	s_mov_b64 s[0:1], 0
	v_mov_b32_e32 v4, v5
	global_load_dwordx4 v[64:67], v[12:13], off
	global_load_dwordx4 v[60:63], v[12:13], off offset:-16
	v_lshl_add_u64 v[20:21], s[8:9], 0, v[10:11]
	v_lshl_add_u64 v[28:29], s[8:9], 0, v[2:3]
	v_lshl_add_u64 v[30:31], s[8:9], 0, v[6:7]
	v_lshl_add_u64 v[32:33], s[8:9], 0, v[8:9]
	global_load_dword v68, v[20:21], off offset:-1024
	global_load_dword v69, v[20:21], off
	global_load_dword v70, v[28:29], off offset:-1024
	global_load_dword v71, v[28:29], off
	global_load_dword v72, v[30:31], off offset:-1024
	global_load_dword v73, v[30:31], off
	global_load_dword v74, v[32:33], off offset:-1024
	global_load_dword v75, v[32:33], off
	s_add_u32 s8, s8, 0x2000
	s_addc_u32 s9, s9, 0
	v_lshl_add_u64 v[12:13], v[12:13], 0, 32
	global_load_dwordx4 v[80:83], v[12:13], off
	global_load_dwordx4 v[76:79], v[12:13], off offset:-16
	v_lshl_add_u64 v[20:21], s[8:9], 0, v[10:11]
	v_lshl_add_u64 v[28:29], s[8:9], 0, v[2:3]
	v_lshl_add_u64 v[30:31], s[8:9], 0, v[6:7]
	v_lshl_add_u64 v[32:33], s[8:9], 0, v[8:9]
	global_load_dword v84, v[20:21], off offset:-1024
	global_load_dword v85, v[20:21], off
	global_load_dword v86, v[28:29], off offset:-1024
	global_load_dword v87, v[28:29], off
	global_load_dword v88, v[30:31], off offset:-1024
	global_load_dword v89, v[30:31], off
	global_load_dword v90, v[32:33], off offset:-1024
	global_load_dword v91, v[32:33], off
	s_add_u32 s8, s8, 0x2000
	s_addc_u32 s9, s9, 0
	v_lshl_add_u64 v[12:13], v[12:13], 0, 32
	global_load_dwordx4 v[96:99], v[12:13], off
	global_load_dwordx4 v[92:95], v[12:13], off offset:-16
	v_lshl_add_u64 v[20:21], s[8:9], 0, v[10:11]
	v_lshl_add_u64 v[28:29], s[8:9], 0, v[2:3]
	v_lshl_add_u64 v[30:31], s[8:9], 0, v[6:7]
	v_lshl_add_u64 v[32:33], s[8:9], 0, v[8:9]
	global_load_dword v100, v[20:21], off offset:-1024
	global_load_dword v101, v[20:21], off
	global_load_dword v102, v[28:29], off offset:-1024
	global_load_dword v103, v[28:29], off
	global_load_dword v104, v[30:31], off offset:-1024
	global_load_dword v105, v[30:31], off
	global_load_dword v106, v[32:33], off offset:-1024
	global_load_dword v107, v[32:33], off
	s_add_u32 s8, s8, 0x2000
	s_addc_u32 s9, s9, 0
	v_lshl_add_u64 v[12:13], v[12:13], 0, 32
	global_load_dwordx4 v[112:115], v[12:13], off
	global_load_dwordx4 v[108:111], v[12:13], off offset:-16
	v_lshl_add_u64 v[20:21], s[8:9], 0, v[10:11]
	v_lshl_add_u64 v[28:29], s[8:9], 0, v[2:3]
	v_lshl_add_u64 v[30:31], s[8:9], 0, v[6:7]
	v_lshl_add_u64 v[32:33], s[8:9], 0, v[8:9]
	global_load_dword v116, v[20:21], off offset:-1024
	global_load_dword v117, v[20:21], off
	global_load_dword v118, v[28:29], off offset:-1024
	global_load_dword v119, v[28:29], off
	global_load_dword v120, v[30:31], off offset:-1024
	global_load_dword v121, v[30:31], off
	global_load_dword v122, v[32:33], off offset:-1024
	global_load_dword v123, v[32:33], off
	s_add_u32 s8, s8, 0x2000
	s_addc_u32 s9, s9, 0
	v_lshl_add_u64 v[12:13], v[12:13], 0, 32
	s_waitcnt vmcnt(30)
	v_pk_fma_f32 v[4:5], v[60:61], v[68:69], v[4:5]
	v_pk_fma_f32 v[4:5], v[62:63], v[70:71], v[4:5]
	v_pk_fma_f32 v[4:5], v[64:65], v[72:73], v[4:5]
	v_pk_fma_f32 v[4:5], v[66:67], v[74:75], v[4:5]
	global_load_dwordx4 v[64:67], v[12:13], off
	global_load_dwordx4 v[60:63], v[12:13], off offset:-16
	v_lshl_add_u64 v[20:21], s[8:9], 0, v[10:11]
	v_lshl_add_u64 v[28:29], s[8:9], 0, v[2:3]
	v_lshl_add_u64 v[30:31], s[8:9], 0, v[6:7]
	v_lshl_add_u64 v[32:33], s[8:9], 0, v[8:9]
	global_load_dword v68, v[20:21], off offset:-1024
	global_load_dword v69, v[20:21], off
	global_load_dword v70, v[28:29], off offset:-1024
	global_load_dword v71, v[28:29], off
	global_load_dword v72, v[30:31], off offset:-1024
	global_load_dword v73, v[30:31], off
	global_load_dword v74, v[32:33], off offset:-1024
	global_load_dword v75, v[32:33], off
	s_add_u32 s8, s8, 0x2000
	s_addc_u32 s9, s9, 0
	v_lshl_add_u64 v[12:13], v[12:13], 0, 32
	s_waitcnt vmcnt(30)
	v_pk_fma_f32 v[4:5], v[76:77], v[84:85], v[4:5]
	v_pk_fma_f32 v[4:5], v[78:79], v[86:87], v[4:5]
	v_pk_fma_f32 v[4:5], v[80:81], v[88:89], v[4:5]
	v_pk_fma_f32 v[4:5], v[82:83], v[90:91], v[4:5]
	global_load_dwordx4 v[80:83], v[12:13], off
	global_load_dwordx4 v[76:79], v[12:13], off offset:-16
	v_lshl_add_u64 v[20:21], s[8:9], 0, v[10:11]
	v_lshl_add_u64 v[28:29], s[8:9], 0, v[2:3]
	v_lshl_add_u64 v[30:31], s[8:9], 0, v[6:7]
	v_lshl_add_u64 v[32:33], s[8:9], 0, v[8:9]
	global_load_dword v84, v[20:21], off offset:-1024
	global_load_dword v85, v[20:21], off
	global_load_dword v86, v[28:29], off offset:-1024
	global_load_dword v87, v[28:29], off
	global_load_dword v88, v[30:31], off offset:-1024
	global_load_dword v89, v[30:31], off
	global_load_dword v90, v[32:33], off offset:-1024
	global_load_dword v91, v[32:33], off
	s_add_u32 s8, s8, 0x2000
	s_addc_u32 s9, s9, 0
	v_lshl_add_u64 v[12:13], v[12:13], 0, 32
	s_waitcnt vmcnt(30)
	v_pk_fma_f32 v[4:5], v[92:93], v[100:101], v[4:5]
	v_pk_fma_f32 v[4:5], v[94:95], v[102:103], v[4:5]
	v_pk_fma_f32 v[4:5], v[96:97], v[104:105], v[4:5]
	v_pk_fma_f32 v[4:5], v[98:99], v[106:107], v[4:5]
	global_load_dwordx4 v[96:99], v[12:13], off
	global_load_dwordx4 v[92:95], v[12:13], off offset:-16
	v_lshl_add_u64 v[20:21], s[8:9], 0, v[10:11]
	v_lshl_add_u64 v[28:29], s[8:9], 0, v[2:3]
	v_lshl_add_u64 v[30:31], s[8:9], 0, v[6:7]
	v_lshl_add_u64 v[32:33], s[8:9], 0, v[8:9]
	global_load_dword v100, v[20:21], off offset:-1024
	global_load_dword v101, v[20:21], off
	global_load_dword v102, v[28:29], off offset:-1024
	global_load_dword v103, v[28:29], off
	global_load_dword v104, v[30:31], off offset:-1024
	global_load_dword v105, v[30:31], off
	global_load_dword v106, v[32:33], off offset:-1024
	global_load_dword v107, v[32:33], off
	s_add_u32 s8, s8, 0x2000
	s_addc_u32 s9, s9, 0
	v_lshl_add_u64 v[12:13], v[12:13], 0, 32
	s_waitcnt vmcnt(30)
	v_pk_fma_f32 v[4:5], v[108:109], v[116:117], v[4:5]
	v_pk_fma_f32 v[4:5], v[110:111], v[118:119], v[4:5]
	v_pk_fma_f32 v[4:5], v[112:113], v[120:121], v[4:5]
	v_pk_fma_f32 v[4:5], v[114:115], v[122:123], v[4:5]
	global_load_dwordx4 v[112:115], v[12:13], off
	global_load_dwordx4 v[108:111], v[12:13], off offset:-16
	v_lshl_add_u64 v[20:21], s[8:9], 0, v[10:11]
	v_lshl_add_u64 v[28:29], s[8:9], 0, v[2:3]
	v_lshl_add_u64 v[30:31], s[8:9], 0, v[6:7]
	v_lshl_add_u64 v[32:33], s[8:9], 0, v[8:9]
	global_load_dword v116, v[20:21], off offset:-1024
	global_load_dword v117, v[20:21], off
	global_load_dword v118, v[28:29], off offset:-1024
	global_load_dword v119, v[28:29], off
	global_load_dword v120, v[30:31], off offset:-1024
	global_load_dword v121, v[30:31], off
	global_load_dword v122, v[32:33], off offset:-1024
	global_load_dword v123, v[32:33], off
	s_add_u32 s8, s8, 0x2000
	s_addc_u32 s9, s9, 0
	v_lshl_add_u64 v[12:13], v[12:13], 0, 32
	s_waitcnt vmcnt(30)
	v_pk_fma_f32 v[4:5], v[60:61], v[68:69], v[4:5]
	v_pk_fma_f32 v[4:5], v[62:63], v[70:71], v[4:5]
	v_pk_fma_f32 v[4:5], v[64:65], v[72:73], v[4:5]
	v_pk_fma_f32 v[4:5], v[66:67], v[74:75], v[4:5]
	s_waitcnt vmcnt(20)
	v_pk_fma_f32 v[4:5], v[76:77], v[84:85], v[4:5]
	v_pk_fma_f32 v[4:5], v[78:79], v[86:87], v[4:5]
	v_pk_fma_f32 v[4:5], v[80:81], v[88:89], v[4:5]
	v_pk_fma_f32 v[4:5], v[82:83], v[90:91], v[4:5]
	s_waitcnt vmcnt(10)
	v_pk_fma_f32 v[4:5], v[92:93], v[100:101], v[4:5]
	v_pk_fma_f32 v[4:5], v[94:95], v[102:103], v[4:5]
	v_pk_fma_f32 v[4:5], v[96:97], v[104:105], v[4:5]
	v_pk_fma_f32 v[4:5], v[98:99], v[106:107], v[4:5]
	s_waitcnt vmcnt(0)
	v_pk_fma_f32 v[4:5], v[108:109], v[116:117], v[4:5]
	v_pk_fma_f32 v[4:5], v[110:111], v[118:119], v[4:5]
	v_pk_fma_f32 v[4:5], v[112:113], v[120:121], v[4:5]
	v_pk_fma_f32 v[4:5], v[114:115], v[122:123], v[4:5]
	s_or_b64 exec, exec, s[0:1]
	s_movk_i32 s0, 0xff
	v_add_f32_e32 v2, v4, v5
	v_cmp_lt_u32_e32 vcc, s0, v0
	ds_write_b32 v14, v2 offset:4096
	s_waitcnt lgkmcnt(0)
	s_barrier
	s_and_saveexec_b64 s[0:1], vcc
	s_xor_b64 s[0:1], exec, s[0:1]
	s_cbranch_execz .LBB12_21
	v_cmp_eq_u32_e32 vcc, 1, v1
	s_and_saveexec_b64 s[8:9], vcc
	s_cbranch_execz .LBB12_20
	v_mov_b32_e32 v1, 2
	v_lshlrev_b32_sdwa v6, v1, v0 dst_sel:DWORD dst_unused:UNUSED_PAD src0_sel:DWORD src1_sel:BYTE_0
	global_load_dword v7, v6, s[6:7]
	ds_read2st64_b32 v[0:1], v6 offset0:16 offset1:20
	ds_read2st64_b32 v[2:3], v6 offset0:24 offset1:28
	s_waitcnt lgkmcnt(1)
	v_mov_b32_e32 v4, v0
	s_waitcnt lgkmcnt(0)
	v_mov_b32_e32 v5, v2
	v_mov_b32_e32 v2, v1
	v_pk_add_f32 v[0:1], v[4:5], v[2:3]
	s_waitcnt vmcnt(0)
	v_add_f32_e32 v0, v7, v0
	v_add_f32_e32 v0, v0, v1
	global_store_dword v6, v0, s[4:5]
